# LDS-DMA: W2 and b2 staged to LDS with global_load_lds_dword in K3 prologue
# baseline (speedup 1.0000x reference)
.LBB2_2:
	s_or_b64 exec, exec, s[4:5]
	s_load_dwordx8 s[48:55], s[0:1], 0x30
	s_load_dwordx2 s[46:47], s[0:1], 0x0
	s_load_dwordx8 s[56:63], s[0:1], 0x10
	s_and_b32 s3, s2, 7
	s_mul_i32 s4, s3, 31
	s_min_u32 s3, s3, 2
	s_ashr_i32 s2, s2, 3
	s_mov_b32 s83, s2
	v_and_b32_e32 v45, 63, v0
	s_add_i32 s64, s3, s2
	v_lshrrev_b32_e32 v6, 6, v0
	s_add_i32 s64, s64, s4
	v_cmp_gt_u32_e64 s[4:5], 16, v45
	v_mov_b32_e32 v4, 0
	v_mov_b32_e32 v2, 0
	v_mov_b32_e32 v3, 0
	s_load_dwordx2 s[6:7], s[0:1], 0x8
	v_lshlrev_b32_e32 v50, 2, v0
	s_movk_i32 s2, 0x280
	v_cmp_gt_u32_e32 vcc, s2, v0
	s_waitcnt lgkmcnt(0)
	v_readfirstlane_b32 s8, v6
	s_lshl_b32 s8, s8, 8
	s_add_i32 s8, s8, 0x16400
	s_mov_b32 m0, s8
	s_and_saveexec_b64 s[2:3], vcc
	s_cbranch_execz .Lpro_a
	global_load_lds_dword v50, s[48:49]
.Lpro_a:
	s_or_b64 exec, exec, s[2:3]
	v_cmp_gt_u32_e32 vcc, 40, v0
	s_mov_b32 m0, 0x17c50
	s_and_saveexec_b64 s[2:3], vcc
	s_cbranch_execz .Lpro_b
	global_load_lds_dword v50, s[50:51]

.LBB2_12:
.LBB2_14:
	s_and_saveexec_b64 s[2:3], s[4:5]
	s_movk_i32 s6, 0x30d4
	v_lshlrev_b32_e32 v5, 2, v102
	v_add_u32_e32 v7, 0x17850, v5
	v_add_u32_e32 v5, 0x17450, v5
	v_mad_u32_u24 v1, v102, s6, v2
	v_sub_u32_e32 v8, v3, v2
	ds_write_b32 v7, v1
	ds_write_b32 v5, v8
	s_or_b64 exec, exec, s[2:3]
	v_readfirstlane_b32 s86, v6
	v_lshlrev_b32_e32 v48, 4, v6
	v_lshlrev_b32_e32 v83, 2, v45
	s_mul_i32 s86, s86, 0xc3500
	s_add_u32 s86, s46, s86
	s_addc_u32 s87, s47, 0
	s_mov_b32 s94, 0
	s_mov_b32 s75, 0
	s_mov_b32 s82, 0
	s_mov_b32 s95, 0
	s_mov_b32 s32, 0
	v_readlane_b32 s2, v2, 0
	v_readlane_b32 s3, v3, 0
	v_readlane_b32 s84, v2, 1
	v_readlane_b32 s85, v3, 1
	s_sub_i32 s42, s3, s2
	s_lshl_b32 s2, s2, 2
	s_add_u32 s88, s86, s2
	s_addc_u32 s89, s87, 0
	v_cmp_gt_u32_e64 s[20:21], s42, v45
	global_load_dword v18, v83, s[88:89]
	s_cmp_le_u32 s42, 64
	s_cbranch_scc1 .Lag_n0
	s_cmp_eq_u32 s94, 0
	s_cbranch_scc0 .Lag_0_1
	s_add_u32 s76, s88, 0x100
	s_addc_u32 s77, s89, 0
	s_sub_i32 s75, s42, 64
	s_branch .Lag_0_e
